# p_mpost token loop: all four heads' loads issued up front, four wave sums as one interleaved butterfly (arithmetic unchanged), on top of v3
# speedup vs baseline: 1.1804x; 1.0040x over previous
.LBB0_1774:
	s_andn2_b64 vcc, exec, s[0:1]
	s_cbranch_vccnz .LBB0_1824
	v_readlane_b32 s0, v254, 9
	s_mov_b32 s0, -1
	v_readlane_b32 s14, v255, 0
	v_mbcnt_lo_u32_b32 v0, s0, 0
	v_mbcnt_hi_u32_b32 v0, s0, v0
	s_mov_b64 s[0:1], s[42:43]
	s_load_dwordx2 s[0:1], s[0:1], 0x68
	v_readlane_b32 s15, v255, 1
	s_add_u32 s7, s14, 0x49500000
	v_readlane_b32 s2, v254, 53
	s_addc_u32 s8, s15, 0
	s_lshl_b32 s2, s2, 12
	s_waitcnt vmcnt(0)
	v_and_b32_e32 v6, 63, v0
	s_waitcnt lgkmcnt(0)
	s_add_u32 s0, s0, s2
	s_addc_u32 s1, s1, 0
	v_lshlrev_b32_e32 v0, 4, v6
	v_lshl_add_u64 v[2:3], s[0:1], 0, v[0:1]
	v_and_b32_e32 v0, 64, v234
	v_add_u32_e32 v0, 64, v0
	v_xor_b32_e32 v5, 1, v234
	v_cmp_lt_i32_e32 vcc, v5, v0
	v_xor_b32_e32 v7, 2, v234
	s_mov_b32 s6, 0
	v_cndmask_b32_e32 v5, v234, v5, vcc
	v_cmp_lt_i32_e32 vcc, v7, v0
	v_lshlrev_b32_e32 v5, 2, v5
	v_readlane_b32 s9, v254, 49
	v_cndmask_b32_e32 v7, v234, v7, vcc
	v_lshlrev_b32_e32 v8, 2, v7
	v_xor_b32_e32 v7, 4, v234
	v_cmp_lt_i32_e32 vcc, v7, v0
	s_mov_b32 s12, 0xf800000
	v_readlane_b32 s3, v254, 54
	v_cndmask_b32_e32 v7, v234, v7, vcc
	v_lshlrev_b32_e32 v9, 2, v7
	v_xor_b32_e32 v7, 8, v234
	v_cmp_lt_i32_e32 vcc, v7, v0
	s_nop 1
	v_cndmask_b32_e32 v7, v234, v7, vcc
	v_lshlrev_b32_e32 v10, 2, v7
	v_xor_b32_e32 v7, 16, v234
	v_cmp_lt_i32_e32 vcc, v7, v0
	s_nop 1
	v_cndmask_b32_e32 v7, v234, v7, vcc
	v_lshlrev_b32_e32 v11, 2, v7
	v_xor_b32_e32 v7, 32, v234
	v_cmp_lt_i32_e32 vcc, v7, v0
	s_nop 1
	v_cndmask_b32_e32 v0, v234, v7, vcc
	v_lshlrev_b32_e32 v12, 2, v0
	v_lshlrev_b32_e32 v0, 3, v6
	global_load_dwordx4 v[140:143], v[2:3], off
	global_load_dwordx4 v[144:147], v[2:3], off offset:1024
	global_load_dwordx4 v[148:151], v[2:3], off offset:2048
	global_load_dwordx4 v[152:155], v[2:3], off offset:3072
.LBB0_1776:
	s_add_i32 s0, s9, s6
	s_ashr_i32 s1, s0, 31
	s_lshl_b64 s[2:3], s[0:1], 11
	s_add_u32 s4, s7, s2
	s_addc_u32 s5, s8, s3
	s_mul_hi_i32 s1, s0, 0x5000
	s_mulk_i32 s0, 0x5000
	s_add_u32 s10, s14, s0
	s_addc_u32 s11, s15, s1
	s_add_u32 s10, s10, 0x33502680
	s_addc_u32 s11, s11, 0
	s_add_u32 s0, s21, s2
	s_addc_u32 s1, s26, s3
	global_load_dwordx2 v[32:33], v0, s[4:5]
	global_load_dwordx2 v[34:35], v0, s[4:5] offset:512
	global_load_dwordx2 v[36:37], v0, s[4:5] offset:1024
	global_load_dwordx2 v[38:39], v0, s[4:5] offset:1536
	global_load_dwordx2 v[40:41], v0, s[10:11]
	global_load_dwordx2 v[42:43], v0, s[10:11] offset:512
	global_load_dwordx2 v[44:45], v0, s[10:11] offset:1024
	global_load_dwordx2 v[46:47], v0, s[10:11] offset:1536
	s_waitcnt vmcnt(7)
	v_lshlrev_b32_e32 v48, 16, v32
	v_and_b32_e32 v49, 0xffff0000, v32
	v_lshlrev_b32_e32 v50, 16, v33
	v_and_b32_e32 v51, 0xffff0000, v33
	v_pk_mul_f32 v[18:19], v[48:49], v[48:49]
	v_pk_mul_f32 v[26:27], v[50:51], v[50:51]
	v_add_f32_e32 v112, v18, v19
	v_add_f32_e32 v112, v26, v112
	v_add_f32_e32 v112, v27, v112
	s_waitcnt vmcnt(6)
	v_lshlrev_b32_e32 v52, 16, v34
	v_and_b32_e32 v53, 0xffff0000, v34
	v_lshlrev_b32_e32 v54, 16, v35
	v_and_b32_e32 v55, 0xffff0000, v35
	v_pk_mul_f32 v[18:19], v[52:53], v[52:53]
	v_pk_mul_f32 v[26:27], v[54:55], v[54:55]
	v_add_f32_e32 v113, v18, v19
	v_add_f32_e32 v113, v26, v113
	v_add_f32_e32 v113, v27, v113
	s_waitcnt vmcnt(5)
	v_lshlrev_b32_e32 v56, 16, v36
	v_and_b32_e32 v57, 0xffff0000, v36
	v_lshlrev_b32_e32 v58, 16, v37
	v_and_b32_e32 v59, 0xffff0000, v37
	v_pk_mul_f32 v[18:19], v[56:57], v[56:57]
	v_pk_mul_f32 v[26:27], v[58:59], v[58:59]
	v_add_f32_e32 v114, v18, v19
	v_add_f32_e32 v114, v26, v114
	v_add_f32_e32 v114, v27, v114
	s_waitcnt vmcnt(4)
	v_lshlrev_b32_e32 v60, 16, v38
	v_and_b32_e32 v61, 0xffff0000, v38
	v_lshlrev_b32_e32 v62, 16, v39
	v_and_b32_e32 v63, 0xffff0000, v39
	v_pk_mul_f32 v[18:19], v[60:61], v[60:61]
	v_pk_mul_f32 v[26:27], v[62:63], v[62:63]
	v_add_f32_e32 v115, v18, v19
	v_add_f32_e32 v115, v26, v115
	v_add_f32_e32 v115, v27, v115
	ds_bpermute_b32 v116, v5, v112
	ds_bpermute_b32 v117, v5, v113
	ds_bpermute_b32 v118, v5, v114
	ds_bpermute_b32 v119, v5, v115
	s_waitcnt vmcnt(3)
	v_lshlrev_b32_e32 v13, 16, v40
	v_and_b32_e32 v30, 0xffff0000, v40
	v_lshlrev_b32_e32 v14, 16, v41
	v_and_b32_e32 v15, 0xffff0000, v41
	v_mul_f32_e32 v13, 0xbfb8aa3b, v13
	v_mul_f32_e32 v30, 0xbfb8aa3b, v30
	v_mul_f32_e32 v14, 0xbfb8aa3b, v14
	v_mul_f32_e32 v15, 0xbfb8aa3b, v15
	v_exp_f32_e32 v13, v13
	v_exp_f32_e32 v30, v30
	v_exp_f32_e32 v14, v14
	v_exp_f32_e32 v15, v15
	s_nop 0
	v_add_f32_e32 v13, 1.0, v13
	v_add_f32_e32 v30, 1.0, v30
	v_add_f32_e32 v14, 1.0, v14
	v_add_f32_e32 v15, 1.0, v15
	v_rcp_f32_e32 v96, v13
	v_rcp_f32_e32 v97, v30
	v_rcp_f32_e32 v98, v14
	v_rcp_f32_e32 v99, v15
	s_waitcnt lgkmcnt(0)
	v_add_f32_e32 v112, v112, v116
	v_add_f32_e32 v113, v113, v117
	v_add_f32_e32 v114, v114, v118
	v_add_f32_e32 v115, v115, v119
	ds_bpermute_b32 v116, v8, v112
	ds_bpermute_b32 v117, v8, v113
	ds_bpermute_b32 v118, v8, v114
	ds_bpermute_b32 v119, v8, v115
	s_waitcnt vmcnt(2)
	v_lshlrev_b32_e32 v13, 16, v42
	v_and_b32_e32 v30, 0xffff0000, v42
	v_lshlrev_b32_e32 v14, 16, v43
	v_and_b32_e32 v15, 0xffff0000, v43
	v_mul_f32_e32 v13, 0xbfb8aa3b, v13
	v_mul_f32_e32 v30, 0xbfb8aa3b, v30
	v_mul_f32_e32 v14, 0xbfb8aa3b, v14
	v_mul_f32_e32 v15, 0xbfb8aa3b, v15
	v_exp_f32_e32 v13, v13
	v_exp_f32_e32 v30, v30
	v_exp_f32_e32 v14, v14
	v_exp_f32_e32 v15, v15
	s_nop 0
	v_add_f32_e32 v13, 1.0, v13
	v_add_f32_e32 v30, 1.0, v30
	v_add_f32_e32 v14, 1.0, v14
	v_add_f32_e32 v15, 1.0, v15
	v_rcp_f32_e32 v100, v13
	v_rcp_f32_e32 v101, v30
	v_rcp_f32_e32 v102, v14
	v_rcp_f32_e32 v103, v15
	s_waitcnt lgkmcnt(0)
	v_add_f32_e32 v112, v112, v116
	v_add_f32_e32 v113, v113, v117
	v_add_f32_e32 v114, v114, v118
	v_add_f32_e32 v115, v115, v119
	ds_bpermute_b32 v116, v9, v112
	ds_bpermute_b32 v117, v9, v113
	ds_bpermute_b32 v118, v9, v114
	ds_bpermute_b32 v119, v9, v115
	s_waitcnt vmcnt(1)
	v_lshlrev_b32_e32 v13, 16, v44
	v_and_b32_e32 v30, 0xffff0000, v44
	v_lshlrev_b32_e32 v14, 16, v45
	v_and_b32_e32 v15, 0xffff0000, v45
	v_mul_f32_e32 v13, 0xbfb8aa3b, v13
	v_mul_f32_e32 v30, 0xbfb8aa3b, v30
	v_mul_f32_e32 v14, 0xbfb8aa3b, v14
	v_mul_f32_e32 v15, 0xbfb8aa3b, v15
	v_exp_f32_e32 v13, v13
	v_exp_f32_e32 v30, v30
	v_exp_f32_e32 v14, v14
	v_exp_f32_e32 v15, v15
	s_nop 0
	v_add_f32_e32 v13, 1.0, v13
	v_add_f32_e32 v30, 1.0, v30
	v_add_f32_e32 v14, 1.0, v14
	v_add_f32_e32 v15, 1.0, v15
	v_rcp_f32_e32 v104, v13
	v_rcp_f32_e32 v105, v30
	v_rcp_f32_e32 v106, v14
	v_rcp_f32_e32 v107, v15
	s_waitcnt lgkmcnt(0)
	v_add_f32_e32 v112, v112, v116
	v_add_f32_e32 v113, v113, v117
	v_add_f32_e32 v114, v114, v118
	v_add_f32_e32 v115, v115, v119
	ds_bpermute_b32 v116, v10, v112
	ds_bpermute_b32 v117, v10, v113
	ds_bpermute_b32 v118, v10, v114
	ds_bpermute_b32 v119, v10, v115
	s_waitcnt vmcnt(0)
	v_lshlrev_b32_e32 v13, 16, v46
	v_and_b32_e32 v30, 0xffff0000, v46
	v_lshlrev_b32_e32 v14, 16, v47
	v_and_b32_e32 v15, 0xffff0000, v47
	v_mul_f32_e32 v13, 0xbfb8aa3b, v13
	v_mul_f32_e32 v30, 0xbfb8aa3b, v30
	v_mul_f32_e32 v14, 0xbfb8aa3b, v14
	v_mul_f32_e32 v15, 0xbfb8aa3b, v15
	v_exp_f32_e32 v13, v13
	v_exp_f32_e32 v30, v30
	v_exp_f32_e32 v14, v14
	v_exp_f32_e32 v15, v15
	s_nop 0
	v_add_f32_e32 v13, 1.0, v13
	v_add_f32_e32 v30, 1.0, v30
	v_add_f32_e32 v14, 1.0, v14
	v_add_f32_e32 v15, 1.0, v15
	v_rcp_f32_e32 v108, v13
	v_rcp_f32_e32 v109, v30
	v_rcp_f32_e32 v110, v14
	v_rcp_f32_e32 v111, v15
	s_waitcnt lgkmcnt(0)
	v_add_f32_e32 v112, v112, v116
	v_add_f32_e32 v113, v113, v117
	v_add_f32_e32 v114, v114, v118
	v_add_f32_e32 v115, v115, v119
	ds_bpermute_b32 v116, v11, v112
	ds_bpermute_b32 v117, v11, v113
	ds_bpermute_b32 v118, v11, v114
	ds_bpermute_b32 v119, v11, v115
	s_waitcnt lgkmcnt(0)
	v_add_f32_e32 v112, v112, v116
	v_add_f32_e32 v113, v113, v117
	v_add_f32_e32 v114, v114, v118
	v_add_f32_e32 v115, v115, v119
	ds_bpermute_b32 v116, v12, v112
	ds_bpermute_b32 v117, v12, v113
	ds_bpermute_b32 v118, v12, v114
	ds_bpermute_b32 v119, v12, v115
	s_waitcnt lgkmcnt(0)
	v_add_f32_e32 v112, v112, v116
	v_add_f32_e32 v113, v113, v117
	v_add_f32_e32 v114, v114, v118
	v_add_f32_e32 v115, v115, v119
	v_fmamk_f32 v13, v112, 0x3b800000, v230
	v_cmp_gt_f32_e32 vcc, s12, v13
	v_mul_f32_e32 v18, 0x4f800000, v13
	s_nop 0
	v_cndmask_b32_e32 v13, v13, v18, vcc
	v_sqrt_f32_e32 v18, v13
	s_nop 0
	v_add_u32_e32 v19, -1, v18
	v_fma_f32 v26, -v19, v18, v13
	v_cmp_ge_f32_e64 s[2:3], 0, v26
	v_add_u32_e32 v26, 1, v18
	s_nop 0
	v_cndmask_b32_e64 v19, v18, v19, s[2:3]
	v_fma_f32 v18, -v26, v18, v13
	v_cmp_lt_f32_e64 s[2:3], 0, v18
	s_nop 1
	v_cndmask_b32_e64 v18, v19, v26, s[2:3]
	v_mul_f32_e32 v19, 0x37800000, v18
	v_cndmask_b32_e32 v18, v18, v19, vcc
	v_cmp_class_f32_e32 vcc, v13, v231
	s_nop 1
	v_cndmask_b32_e32 v13, v18, v13, vcc
	v_div_scale_f32 v18, s[2:3], v13, v13, 1.0
	v_rcp_f32_e32 v19, v18
	s_nop 0
	v_fma_f32 v26, -v18, v19, 1.0
	v_fmac_f32_e32 v19, v26, v19
	v_div_scale_f32 v26, vcc, 1.0, v13, 1.0
	v_mul_f32_e32 v27, v26, v19
	v_fma_f32 v30, -v18, v27, v26
	v_fmac_f32_e32 v27, v30, v19
	v_fma_f32 v18, -v18, v27, v26
	v_div_fmas_f32 v18, v18, v19, v27
	v_div_fixup_f32 v120, v18, v13, 1.0
	v_pk_mul_f32 v[156:157], v[120:121], v[48:49] op_sel_hi:[0,1]
	v_pk_mul_f32 v[158:159], v[120:121], v[50:51] op_sel_hi:[0,1]
	v_pk_mul_f32 v[156:157], v[140:141], v[156:157]
	v_pk_mul_f32 v[158:159], v[142:143], v[158:159]
	v_pk_mul_f32 v[156:157], v[96:97], v[156:157]
	v_pk_mul_f32 v[158:159], v[98:99], v[158:159]
	v_cvt_pk_bf16_f32 v156, v156, v157
	v_cvt_pk_bf16_f32 v157, v158, v159
	global_store_dwordx2 v0, v[156:157], s[0:1]
	v_fmamk_f32 v13, v113, 0x3b800000, v230
	v_cmp_gt_f32_e32 vcc, s12, v13
	v_mul_f32_e32 v18, 0x4f800000, v13
	s_nop 0
	v_cndmask_b32_e32 v13, v13, v18, vcc
	v_sqrt_f32_e32 v18, v13
	s_nop 0
	v_add_u32_e32 v19, -1, v18
	v_fma_f32 v26, -v19, v18, v13
	v_cmp_ge_f32_e64 s[2:3], 0, v26
	v_add_u32_e32 v26, 1, v18
	s_nop 0
	v_cndmask_b32_e64 v19, v18, v19, s[2:3]
	v_fma_f32 v18, -v26, v18, v13
	v_cmp_lt_f32_e64 s[2:3], 0, v18
	s_nop 1
	v_cndmask_b32_e64 v18, v19, v26, s[2:3]
	v_mul_f32_e32 v19, 0x37800000, v18
	v_cndmask_b32_e32 v18, v18, v19, vcc
	v_cmp_class_f32_e32 vcc, v13, v231
	s_nop 1
	v_cndmask_b32_e32 v13, v18, v13, vcc
	v_div_scale_f32 v18, s[2:3], v13, v13, 1.0
	v_rcp_f32_e32 v19, v18
	s_nop 0
	v_fma_f32 v26, -v18, v19, 1.0
	v_fmac_f32_e32 v19, v26, v19
	v_div_scale_f32 v26, vcc, 1.0, v13, 1.0
	v_mul_f32_e32 v27, v26, v19
	v_fma_f32 v30, -v18, v27, v26
	v_fmac_f32_e32 v27, v30, v19
	v_fma_f32 v18, -v18, v27, v26
	v_div_fmas_f32 v18, v18, v19, v27
	v_div_fixup_f32 v122, v18, v13, 1.0
	v_pk_mul_f32 v[160:161], v[122:123], v[52:53] op_sel_hi:[0,1]
	v_pk_mul_f32 v[162:163], v[122:123], v[54:55] op_sel_hi:[0,1]
	v_pk_mul_f32 v[160:161], v[144:145], v[160:161]
	v_pk_mul_f32 v[162:163], v[146:147], v[162:163]
	v_pk_mul_f32 v[160:161], v[100:101], v[160:161]
	v_pk_mul_f32 v[162:163], v[102:103], v[162:163]
	v_cvt_pk_bf16_f32 v160, v160, v161
	v_cvt_pk_bf16_f32 v161, v162, v163
	global_store_dwordx2 v0, v[160:161], s[0:1] offset:512
	v_fmamk_f32 v13, v114, 0x3b800000, v230
	v_cmp_gt_f32_e32 vcc, s12, v13
	v_mul_f32_e32 v18, 0x4f800000, v13
	s_nop 0
	v_cndmask_b32_e32 v13, v13, v18, vcc
	v_sqrt_f32_e32 v18, v13
	s_nop 0
	v_add_u32_e32 v19, -1, v18
	v_fma_f32 v26, -v19, v18, v13
	v_cmp_ge_f32_e64 s[2:3], 0, v26
	v_add_u32_e32 v26, 1, v18
	s_nop 0
	v_cndmask_b32_e64 v19, v18, v19, s[2:3]
	v_fma_f32 v18, -v26, v18, v13
	v_cmp_lt_f32_e64 s[2:3], 0, v18
	s_nop 1
	v_cndmask_b32_e64 v18, v19, v26, s[2:3]
	v_mul_f32_e32 v19, 0x37800000, v18
	v_cndmask_b32_e32 v18, v18, v19, vcc
	v_cmp_class_f32_e32 vcc, v13, v231
	s_nop 1
	v_cndmask_b32_e32 v13, v18, v13, vcc
	v_div_scale_f32 v18, s[2:3], v13, v13, 1.0
	v_rcp_f32_e32 v19, v18
	s_nop 0
	v_fma_f32 v26, -v18, v19, 1.0
	v_fmac_f32_e32 v19, v26, v19
	v_div_scale_f32 v26, vcc, 1.0, v13, 1.0
	v_mul_f32_e32 v27, v26, v19
	v_fma_f32 v30, -v18, v27, v26
	v_fmac_f32_e32 v27, v30, v19
	v_fma_f32 v18, -v18, v27, v26
	v_div_fmas_f32 v18, v18, v19, v27
	v_div_fixup_f32 v124, v18, v13, 1.0
	v_pk_mul_f32 v[164:165], v[124:125], v[56:57] op_sel_hi:[0,1]
	v_pk_mul_f32 v[166:167], v[124:125], v[58:59] op_sel_hi:[0,1]
	v_pk_mul_f32 v[164:165], v[148:149], v[164:165]
	v_pk_mul_f32 v[166:167], v[150:151], v[166:167]
	v_pk_mul_f32 v[164:165], v[104:105], v[164:165]
	v_pk_mul_f32 v[166:167], v[106:107], v[166:167]
	v_cvt_pk_bf16_f32 v164, v164, v165
	v_cvt_pk_bf16_f32 v165, v166, v167
	global_store_dwordx2 v0, v[164:165], s[0:1] offset:1024
	v_fmamk_f32 v13, v115, 0x3b800000, v230
	v_cmp_gt_f32_e32 vcc, s12, v13
	v_mul_f32_e32 v18, 0x4f800000, v13
	s_nop 0
	v_cndmask_b32_e32 v13, v13, v18, vcc
	v_sqrt_f32_e32 v18, v13
	s_nop 0
	v_add_u32_e32 v19, -1, v18
	v_fma_f32 v26, -v19, v18, v13
	v_cmp_ge_f32_e64 s[2:3], 0, v26
	v_add_u32_e32 v26, 1, v18
	s_nop 0
	v_cndmask_b32_e64 v19, v18, v19, s[2:3]
	v_fma_f32 v18, -v26, v18, v13
	v_cmp_lt_f32_e64 s[2:3], 0, v18
	s_nop 1
	v_cndmask_b32_e64 v18, v19, v26, s[2:3]
	v_mul_f32_e32 v19, 0x37800000, v18
	v_cndmask_b32_e32 v18, v18, v19, vcc
	v_cmp_class_f32_e32 vcc, v13, v231
	s_nop 1
	v_cndmask_b32_e32 v13, v18, v13, vcc
	v_div_scale_f32 v18, s[2:3], v13, v13, 1.0
	v_rcp_f32_e32 v19, v18
	s_nop 0
	v_fma_f32 v26, -v18, v19, 1.0
	v_fmac_f32_e32 v19, v26, v19
	v_div_scale_f32 v26, vcc, 1.0, v13, 1.0
	v_mul_f32_e32 v27, v26, v19
	v_fma_f32 v30, -v18, v27, v26
	v_fmac_f32_e32 v27, v30, v19
	v_fma_f32 v18, -v18, v27, v26
	v_div_fmas_f32 v18, v18, v19, v27
	v_div_fixup_f32 v126, v18, v13, 1.0
	v_pk_mul_f32 v[168:169], v[126:127], v[60:61] op_sel_hi:[0,1]
	v_pk_mul_f32 v[170:171], v[126:127], v[62:63] op_sel_hi:[0,1]
	v_pk_mul_f32 v[168:169], v[152:153], v[168:169]
	v_pk_mul_f32 v[170:171], v[154:155], v[170:171]
	v_pk_mul_f32 v[168:169], v[108:109], v[168:169]
	v_pk_mul_f32 v[170:171], v[110:111], v[170:171]
	v_cvt_pk_bf16_f32 v168, v168, v169
	v_cvt_pk_bf16_f32 v169, v170, v171
	global_store_dwordx2 v0, v[168:169], s[0:1] offset:1536
	s_addk_i32 s6, 0x100
	s_cmpk_lg_i32 s6, 0x800
	s_cbranch_scc1 .LBB0_1776
	v_readlane_b32 s0, v254, 57
	s_add_i32 s20, s0, 8
	v_readlane_b32 s0, v254, 5
	s_cmp_ge_i32 s20, s0
	s_cbranch_scc1 .LBB0_1824
	v_readlane_b32 s0, v254, 9
	s_waitcnt vmcnt(0)
	s_barrier
	s_mov_b32 s1, -1
	s_lshl_b32 s0, s0, 6
	v_mbcnt_lo_u32_b32 v0, s1, 0
	v_mbcnt_hi_u32_b32 v0, s1, v0
	s_sub_i32 s0, 0, s0
	v_cmp_eq_u32_e32 vcc, s0, v0
	s_and_saveexec_b64 s[0:1], vcc
	s_cbranch_execz .LBB0_1823
	v_readlane_b32 s2, v254, 6
	v_readlane_b32 s4, v254, 8
	v_readlane_b32 s3, v254, 7
	s_waitcnt vmcnt(0) expcnt(0) lgkmcnt(0)
	v_mov_b32_e32 v0, s4
	ds_read_b32 v2, v0
	ds_read_b32 v0, v0 offset:4
	s_waitcnt lgkmcnt(1)
	v_cmp_ne_u32_e32 vcc, 0, v2
	s_cbranch_vccnz .LBB0_1793
	s_add_u32 s4, s2, 0x1000
	s_addc_u32 s5, s3, 0
	s_add_u32 s6, s2, 0x1100
	s_addc_u32 s7, s3, 0
	s_add_u32 s8, s2, 0x1200
	s_addc_u32 s9, s3, 0
	s_add_u32 s10, s2, 0x1300
	s_addc_u32 s11, s3, 0
	s_mov_b32 s38, 1
	s_mov_b64 s[12:13], 0
	s_branch .LBB0_1783
